# P9 hand-written steady K-loop + deferred gather-offset wait; P2 GEMM workgroups convert last 768 weight tiles after their GEMM
# speedup vs baseline: 1.0154x; 1.0154x over previous
; __global__ void __launch_bounds__(NWAVES * 64, 2) fwd_kernel(Args args) {
;     ...
;         const bool split2 = (G == 256); const int xcd2 = bx & 7, slot2 = bx >> 3;
;         if (!split2 || slot2 < T8_GS) {
;         SchedDense S; S.init(Z_FP8 ? (const void*)XN8 : (const void*)XN, WinT, T, INW, D, D, split2 ? T8_GS * 8 : G, split2 ? slot2 * 8 + xcd2 : bx, Z_FP8 ? 1 : 2);
;         EpiZ E{UP, UG, SGP, SGS, Z_FP8 ? 0.03125f : 1.0f};
;         pg8::gemm_phase<EpiZ, SchedDense, false, Z_FP8 ? 1 : 2>(lds + RING_OFF, D, D, D, S, E);
;         } else { constexpr int TRB = 256 * 144; T8_CONSTS; T8_RUN(U_TOT - T8_NMOVE + (slot2 - T8_GS) * 8 + xcd2, (32 - T8_GS) * 8, U_TOT); }
.LBB0_431:
	s_cmp_lt_i32 s94, 3
	s_cselect_b64 s[4:5], -1, 0
	s_cmp_gt_i32 s95, 2
	s_cselect_b64 s[6:7], -1, 0
	s_and_b64 s[4:5], s[4:5], s[6:7]
	s_andn2_b64 vcc, exec, s[4:5]
	s_cbranch_vccnz .LBB0_615
	v_readlane_b32 s4, v254, 1
	v_readlane_b32 s5, v254, 2
	s_cmpk_lg_i32 s50, 0x100
	s_load_dwordx2 s[8:9], s[4:5], 0xf8
	s_cselect_b64 s[12:13], -1, 0
	s_cmpk_eq_i32 s50, 0x100
	s_cselect_b64 s[6:7], -1, 0
	s_cmpk_gt_i32 s2, 0x7f
	s_cselect_b64 s[10:11], -1, 0
	s_and_b64 s[10:11], s[10:11], s[6:7]
	s_mov_b64 s[6:7], -1
	s_and_b64 vcc, exec, s[10:11]
	s_cbranch_vccz .LBB0_464
	s_movk_i32 s98, 0x2fc0
	s_movk_i32 s99, 0x2f40
	s_movk_i32 s100, 0x2ec0
	s_movk_i32 s101, 0x740
.Lp2_conv_entry:
	s_waitcnt lgkmcnt(0)
	s_add_u32 s3, s8, 0x4400000
	s_addc_u32 s30, s9, 0
	s_load_dwordx2 s[10:11], s[4:5], 0xb8
	s_load_dwordx2 s[16:17], s[4:5], 0xc8
	s_add_u32 s31, s8, 0x24400000
	s_addc_u32 s33, s9, 0
	s_and_b32 s37, s2, 0x7fffffff
	s_add_i32 s37, s37, s101
	s_cmp_lt_i32 s37, s98
	s_mov_b64 s[18:19], 0
	s_mov_b32 s36, 0
	s_cselect_b64 s[6:7], -1, 0
	s_cmp_ge_i32 s37, s98
	v_mov_b32_e32 v1, 0
	s_mov_b32 s59, 0
	s_mov_b32 s62, 0
	v_mov_b32_e32 v130, 0
	s_mov_b32 s60, 0
	s_mov_b32 s61, 0
	s_mov_b64 s[4:5], 0
	s_cbranch_scc1 .LBB0_435
	s_cmpk_lt_i32 s37, 0x22c0
	s_cselect_b64 s[4:5], -1, 0
	s_movk_i32 s14, 0xfd40
	v_cndmask_b32_e64 v130, 0, 1, s[4:5]
	s_and_b64 s[4:5], s[4:5], exec
	s_cselect_b32 s4, s14, 0xffffdd40
	s_movk_i32 s14, 0xff
	s_cselect_b32 s15, s14, 0x7f
	s_movk_i32 s14, 0x1000
	s_cselect_b32 s60, s14, 0x800
	s_mov_b32 s14, 0xc000
	s_cselect_b32 s38, s14, 0x6000
	s_mov_b32 s14, 0x14000
	s_cselect_b32 s40, s14, 0xa000
	s_mov_b32 s14, 0x18000
	s_cselect_b32 s42, s14, 0xc000
	s_mov_b32 s14, 0x1c000
	s_cselect_b32 s44, s14, 0xe000
	s_mov_b32 s14, 0x24000
	s_cselect_b32 s46, s14, 0x12000
	s_mov_b32 s14, 0x28000
	s_cselect_b32 s48, s14, 0x14000
	s_mov_b32 s14, 0x2c000
	s_cselect_b32 s28, s14, 0x16000
	s_mov_b32 s14, 0x30000
	s_cselect_b32 s26, s14, 0x18000
	s_mov_b32 s14, 0x34000
	s_cselect_b32 s24, s14, 0x1a000
	s_mov_b32 s14, 0x38000
	s_cselect_b32 s22, s14, 0x1c000
	s_mov_b32 s14, 0x3c000
	s_cselect_b32 s5, 8, 7
	s_waitcnt lgkmcnt(0)
	s_cselect_b32 s23, s11, s17
	s_cselect_b32 s25, s10, s16
	s_cselect_b32 s27, s30, s33
	s_cselect_b32 s29, s3, s31
	s_cselect_b32 s39, 23, 22
	s_cselect_b32 s41, 4, 3
	s_cselect_b32 s43, 12, 11
	s_cselect_b32 s14, s14, 0x1e000
	s_add_i32 s4, s37, s4
	s_lshr_b32 s20, s4, s5
	s_mov_b32 s21, 0
	s_and_b32 s15, s4, s15
	s_lshl_b64 s[4:5], s[20:21], s39
	s_lshl_b64 s[52:53], s[4:5], 2
	s_add_u32 s25, s25, s52
	s_addc_u32 s23, s23, s53
	s_add_u32 s4, s29, s4
	s_addc_u32 s5, s27, s5
	s_lshr_b32 s20, s60, 8
	s_lshr_b32 s27, s15, s41
	s_add_i32 s20, s20, -1
	v_readlane_b32 s1, v254, 7
	s_lshl_b32 s62, s27, 7
	s_and_b32 s15, s20, s15
	s_lshl_b32 s20, s1, 4
	s_add_i32 s20, s62, s20
	s_lshl_b64 s[52:53], s[20:21], s43
	s_lshl_b32 s59, s15, 8
	s_lshl_b64 s[52:53], s[52:53], 2
	s_add_u32 s20, s25, s52
	s_addc_u32 s23, s23, s53
	s_lshl_b32 s15, s15, 10
	s_add_u32 s52, s20, s15
	s_addc_u32 s53, s23, 0
	s_waitcnt vmcnt(15)
	v_lshlrev_b32_e32 v66, 4, v194
	v_mov_b32_e32 v67, 0
	s_waitcnt vmcnt(0)
	v_lshl_add_u64 v[58:59], s[52:53], 0, v[66:67]
	s_lshl_b32 s20, s60, 2
	v_lshl_add_u64 v[2:3], v[58:59], 0, s[20:21]
	s_lshl_b32 s20, s60, 3
	v_lshl_add_u64 v[6:7], v[58:59], 0, s[20:21]
	s_lshl_b32 s20, s60, 4
	s_mov_b32 s39, s21
	v_lshl_add_u64 v[14:15], v[58:59], 0, s[20:21]
	s_mov_b32 s41, s21
	s_mov_b32 s43, s21
	s_mov_b32 s45, s21
	s_lshl_b32 s20, s60, 5
	s_mov_b32 s47, s21
	s_mov_b32 s49, s21
	s_mov_b32 s29, s21
	s_mov_b32 s27, s21
	s_mov_b32 s25, s21
	s_mov_b32 s23, s21
	v_lshl_add_u64 v[10:11], v[58:59], 0, s[38:39]
	v_lshl_add_u64 v[18:19], v[58:59], 0, s[40:41]
	v_lshl_add_u64 v[22:23], v[58:59], 0, s[42:43]
	v_lshl_add_u64 v[26:27], v[58:59], 0, s[44:45]
	v_lshl_add_u64 v[30:31], v[58:59], 0, s[20:21]
	v_lshl_add_u64 v[34:35], v[58:59], 0, s[46:47]
	v_lshl_add_u64 v[38:39], v[58:59], 0, s[48:49]
	v_lshl_add_u64 v[42:43], v[58:59], 0, s[28:29]
	v_lshl_add_u64 v[46:47], v[58:59], 0, s[26:27]
	v_lshl_add_u64 v[50:51], v[58:59], 0, s[24:25]
	v_lshl_add_u64 v[54:55], v[58:59], 0, s[22:23]
	s_mov_b32 s15, s21
	global_load_dwordx4 v[2:5], v[2:3], off nt
	s_nop 0
	global_load_dwordx4 v[6:9], v[6:7], off nt
	s_nop 0
	global_load_dwordx4 v[10:13], v[10:11], off nt
	s_nop 0
	global_load_dwordx4 v[14:17], v[14:15], off nt
	s_nop 0
	global_load_dwordx4 v[18:21], v[18:19], off nt
	s_nop 0
	global_load_dwordx4 v[22:25], v[22:23], off nt
	s_nop 0
	global_load_dwordx4 v[26:29], v[26:27], off nt
	s_nop 0
	global_load_dwordx4 v[30:33], v[30:31], off nt
	s_nop 0
	global_load_dwordx4 v[34:37], v[34:35], off nt
	s_nop 0
	global_load_dwordx4 v[38:41], v[38:39], off nt
	s_nop 0
	global_load_dwordx4 v[42:45], v[42:43], off nt
	s_nop 0
	global_load_dwordx4 v[46:49], v[46:47], off nt
	s_nop 0
	global_load_dwordx4 v[50:53], v[50:51], off nt
	s_nop 0
	global_load_dwordx4 v[54:57], v[54:55], off nt
	v_lshl_add_u64 v[68:69], v[58:59], 0, s[14:15]
	global_load_dwordx4 v[62:65], v66, s[52:53] nt
	global_load_dwordx4 v[58:61], v[68:69], off nt
	s_movk_i32 s61, 0x800
.LBB0_435:
	s_cmp_ge_i32 s37, s99
	s_mov_b32 s53, 0
	s_mov_b32 s49, 0
	s_mov_b32 s52, 0
	s_cbranch_scc1 .LBB0_437
	s_cmpk_lt_i32 s37, 0x2240
	s_cselect_b64 s[14:15], -1, 0
	v_cndmask_b32_e64 v1, 0, 1, s[14:15]
	s_and_b64 s[14:15], s[14:15], exec
	s_movk_i32 s14, 0xff
	s_cselect_b32 s19, s14, 0x7f
	s_movk_i32 s14, 0x1000
	s_cselect_b32 s49, s14, 0x800
	s_mov_b32 s14, 0xc000
	s_cselect_b32 s38, s14, 0x6000
	s_mov_b32 s14, 0x14000
	s_cselect_b32 s40, s14, 0xa000
	s_mov_b32 s14, 0x18000
	s_cselect_b32 s42, s14, 0xc000
	s_mov_b32 s14, 0x1c000
	s_cselect_b32 s44, s14, 0xe000
	s_mov_b32 s14, 0x24000
	s_cselect_b32 s46, s14, 0x12000
	s_mov_b32 s14, 0x28000
	s_cselect_b32 s54, s14, 0x14000
	s_mov_b32 s14, 0x2c000
	s_cselect_b32 s28, s14, 0x16000
	s_mov_b32 s14, 0x30000
	s_cselect_b32 s26, s14, 0x18000
	s_mov_b32 s14, 0x34000
	s_movk_i32 s18, 0xfdc0
	s_cselect_b32 s24, s14, 0x1a000
	s_mov_b32 s14, 0x38000
	s_cselect_b32 s15, s18, 0xffffddc0
	s_cselect_b32 s22, s14, 0x1c000
	s_mov_b32 s14, 0x3c000
	s_cselect_b32 s18, 8, 7
	s_waitcnt lgkmcnt(0)
	s_cselect_b32 s23, s11, s17
	s_cselect_b32 s25, s10, s16
	s_cselect_b32 s27, s30, s33
	s_cselect_b32 s29, s3, s31
	s_cselect_b32 s36, 23, 22
	s_cselect_b32 s39, 4, 3
	s_cselect_b32 s41, 12, 11
	s_cselect_b32 s14, s14, 0x1e000
	s_add_i32 s15, s37, s15
	s_lshr_b32 s20, s15, s18
	s_mov_b32 s21, 0
	s_and_b32 s15, s15, s19
	s_lshl_b64 s[18:19], s[20:21], s36
	s_lshl_b64 s[52:53], s[18:19], 2
	s_add_u32 s25, s25, s52
	s_addc_u32 s23, s23, s53
	s_add_u32 s18, s29, s18
	s_addc_u32 s19, s27, s19
	s_lshr_b32 s20, s49, 8
	s_lshr_b32 s27, s15, s39
	s_add_i32 s20, s20, -1
	v_readlane_b32 s1, v254, 7
	s_lshl_b32 s53, s27, 7
	s_and_b32 s15, s20, s15
	s_lshl_b32 s20, s1, 4
	s_add_i32 s20, s53, s20
	s_lshl_b64 s[56:57], s[20:21], s41
	s_lshl_b32 s36, s15, 8
	s_lshl_b64 s[56:57], s[56:57], 2
	s_add_u32 s20, s25, s56
	s_addc_u32 s23, s23, s57
	s_lshl_b32 s15, s15, 10
	s_add_u32 s56, s20, s15
	s_addc_u32 s57, s23, 0
	s_waitcnt vmcnt(2)
	v_lshlrev_b32_e32 v122, 4, v194
	v_mov_b32_e32 v123, 0
	v_lshl_add_u64 v[124:125], s[56:57], 0, v[122:123]
	s_lshl_b32 s20, s49, 2
	v_lshl_add_u64 v[66:67], v[124:125], 0, s[20:21]
	s_lshl_b32 s20, s49, 3
	v_lshl_add_u64 v[70:71], v[124:125], 0, s[20:21]
	s_lshl_b32 s20, s49, 4
	s_mov_b32 s39, s21
	v_lshl_add_u64 v[78:79], v[124:125], 0, s[20:21]
	s_mov_b32 s41, s21
	s_mov_b32 s43, s21
	s_mov_b32 s45, s21
	s_lshl_b32 s20, s49, 5
	s_mov_b32 s47, s21
	s_mov_b32 s55, s21
	s_mov_b32 s29, s21
	s_mov_b32 s27, s21
	s_mov_b32 s25, s21
	s_mov_b32 s23, s21
	s_mov_b32 s15, s21
	v_lshl_add_u64 v[74:75], v[124:125], 0, s[38:39]
	v_lshl_add_u64 v[82:83], v[124:125], 0, s[40:41]
	s_waitcnt vmcnt(1)
	v_lshl_add_u64 v[86:87], v[124:125], 0, s[42:43]
	v_lshl_add_u64 v[90:91], v[124:125], 0, s[44:45]
	v_lshl_add_u64 v[94:95], v[124:125], 0, s[20:21]
	v_lshl_add_u64 v[98:99], v[124:125], 0, s[46:47]
	v_lshl_add_u64 v[102:103], v[124:125], 0, s[54:55]
	v_lshl_add_u64 v[106:107], v[124:125], 0, s[28:29]
	v_lshl_add_u64 v[110:111], v[124:125], 0, s[26:27]
	v_lshl_add_u64 v[114:115], v[124:125], 0, s[24:25]
	v_lshl_add_u64 v[118:119], v[124:125], 0, s[22:23]
	s_waitcnt vmcnt(0)
	v_lshl_add_u64 v[126:127], v[124:125], 0, s[14:15]
	global_load_dwordx4 v[66:69], v[66:67], off nt
	s_nop 0
	global_load_dwordx4 v[70:73], v[70:71], off nt
	s_nop 0
	global_load_dwordx4 v[74:77], v[74:75], off nt
	s_nop 0
	global_load_dwordx4 v[78:81], v[78:79], off nt
	s_nop 0
	global_load_dwordx4 v[82:85], v[82:83], off nt
	s_nop 0
	global_load_dwordx4 v[86:89], v[86:87], off nt
	s_nop 0
	global_load_dwordx4 v[90:93], v[90:91], off nt
	s_nop 0
	global_load_dwordx4 v[94:97], v[94:95], off nt
	s_nop 0
	global_load_dwordx4 v[98:101], v[98:99], off nt
	s_nop 0
	global_load_dwordx4 v[102:105], v[102:103], off nt
	s_nop 0
	global_load_dwordx4 v[106:109], v[106:107], off nt
	s_nop 0
	global_load_dwordx4 v[110:113], v[110:111], off nt
	s_nop 0
	global_load_dwordx4 v[114:117], v[114:115], off nt
	s_nop 0
	global_load_dwordx4 v[118:121], v[118:119], off nt
	s_nop 0
	global_load_dwordx4 v[122:125], v122, s[56:57] nt
	s_nop 0
	global_load_dwordx4 v[126:129], v[126:127], off nt
	s_movk_i32 s52, 0x800

.LBB0_441:
	s_waitcnt vmcnt(1)
	v_mul_f32_e32 v131, 0x42000000, v62
	v_mul_f32_e32 v132, 0x42000000, v2
	v_med3_f32 v131, v131, s28, v149
	v_med3_f32 v134, v132, s28, v149
	v_mov_b32_e32 v132, 0
	v_cvt_pk_fp8_f32 v132, v131, v134
	v_mul_f32_e32 v133, 0x42000000, v6
	v_mul_f32_e32 v131, 0x42000000, v10
	v_med3_f32 v133, v133, s28, v149
	v_med3_f32 v131, v131, s28, v149
	v_cvt_pk_fp8_f32 v132, v133, v131 op_sel:[0,0,1]
	v_mul_f32_e32 v131, 0x42000000, v14
	v_mul_f32_e32 v133, 0x42000000, v18
	v_med3_f32 v131, v131, s28, v149
	v_med3_f32 v135, v133, s28, v149
	v_mov_b32_e32 v133, 0
	v_cvt_pk_fp8_f32 v133, v131, v135
	v_mul_f32_e32 v134, 0x42000000, v22
	s_waitcnt vmcnt(0)
	v_mul_f32_e32 v131, 0x42000000, v26
	v_med3_f32 v134, v134, s28, v149
	v_med3_f32 v131, v131, s28, v149
	v_cvt_pk_fp8_f32 v133, v134, v131 op_sel:[0,0,1]
	v_mul_f32_e32 v131, 0x42000000, v30
	v_mul_f32_e32 v134, 0x42000000, v34
	v_med3_f32 v131, v131, s28, v149
	v_med3_f32 v136, v134, s28, v149
	v_mov_b32_e32 v134, 0
	v_cvt_pk_fp8_f32 v134, v131, v136
	v_mul_f32_e32 v135, 0x42000000, v38
	v_mul_f32_e32 v131, 0x42000000, v42
	v_med3_f32 v135, v135, s28, v149
	v_med3_f32 v131, v131, s28, v149
	v_cvt_pk_fp8_f32 v134, v135, v131 op_sel:[0,0,1]
	v_mul_f32_e32 v131, 0x42000000, v46
	v_mul_f32_e32 v135, 0x42000000, v50
	v_med3_f32 v131, v131, s28, v149
	v_med3_f32 v137, v135, s28, v149
	v_mov_b32_e32 v135, 0
	v_cvt_pk_fp8_f32 v135, v131, v137
	v_mul_f32_e32 v136, 0x42000000, v54
	v_mul_f32_e32 v131, 0x42000000, v58
	v_med3_f32 v136, v136, s28, v149
	v_med3_f32 v131, v131, s28, v149
	v_cvt_pk_fp8_f32 v135, v136, v131 op_sel:[0,0,1]
	v_mul_f32_e32 v131, 0x42000000, v63
	v_med3_f32 v131, v131, s28, v149
	v_mov_b32_e32 v154, 0
	ds_write_b128 v150, v[132:135]
	v_mul_f32_e32 v132, 0x42000000, v3
	v_med3_f32 v134, v132, s28, v149
	v_mov_b32_e32 v132, 0
	v_cvt_pk_fp8_f32 v132, v131, v134
	v_mul_f32_e32 v133, 0x42000000, v7
	v_mul_f32_e32 v131, 0x42000000, v11
	v_med3_f32 v133, v133, s28, v149
	v_med3_f32 v131, v131, s28, v149
	v_cvt_pk_fp8_f32 v132, v133, v131 op_sel:[0,0,1]
	v_mul_f32_e32 v131, 0x42000000, v15
	v_mul_f32_e32 v133, 0x42000000, v19
	v_med3_f32 v131, v131, s28, v149
	v_med3_f32 v135, v133, s28, v149
	v_mov_b32_e32 v133, 0
	v_cvt_pk_fp8_f32 v133, v131, v135
	v_mul_f32_e32 v134, 0x42000000, v23
	v_mul_f32_e32 v131, 0x42000000, v27
	v_med3_f32 v134, v134, s28, v149
	v_med3_f32 v131, v131, s28, v149
	v_cvt_pk_fp8_f32 v133, v134, v131 op_sel:[0,0,1]
	v_mul_f32_e32 v131, 0x42000000, v31
	v_mul_f32_e32 v134, 0x42000000, v35
	v_med3_f32 v131, v131, s28, v149
	v_med3_f32 v136, v134, s28, v149
	v_mov_b32_e32 v134, 0
	v_cvt_pk_fp8_f32 v134, v131, v136
	v_mul_f32_e32 v135, 0x42000000, v39
	v_mul_f32_e32 v131, 0x42000000, v43
	v_med3_f32 v135, v135, s28, v149
	v_med3_f32 v131, v131, s28, v149
	v_cvt_pk_fp8_f32 v134, v135, v131 op_sel:[0,0,1]
	v_mul_f32_e32 v131, 0x42000000, v47
	v_mul_f32_e32 v135, 0x42000000, v51
	v_med3_f32 v131, v131, s28, v149
	v_med3_f32 v137, v135, s28, v149
	v_mov_b32_e32 v135, 0
	v_cvt_pk_fp8_f32 v135, v131, v137
	v_mul_f32_e32 v136, 0x42000000, v55
	v_mul_f32_e32 v131, 0x42000000, v59
	v_med3_f32 v136, v136, s28, v149
	v_med3_f32 v131, v131, s28, v149
	v_cvt_pk_fp8_f32 v135, v136, v131 op_sel:[0,0,1]
	v_mul_f32_e32 v131, 0x42000000, v64
	v_mul_f32_e32 v136, 0x42000000, v4
	v_med3_f32 v131, v131, s28, v149
	v_med3_f32 v136, v136, s28, v149
	v_cvt_pk_fp8_f32 v154, v131, v136
	v_mul_f32_e32 v137, 0x42000000, v8
	v_mul_f32_e32 v131, 0x42000000, v12
	v_med3_f32 v136, v137, s28, v149
	v_med3_f32 v131, v131, s28, v149
	v_cvt_pk_fp8_f32 v154, v136, v131 op_sel:[0,0,1]
	v_mul_f32_e32 v131, 0x42000000, v16
	v_mul_f32_e32 v136, 0x42000000, v20
	v_med3_f32 v131, v131, s28, v149
	v_med3_f32 v136, v136, s28, v149
	v_mov_b32_e32 v155, 0
	v_cvt_pk_fp8_f32 v155, v131, v136
	v_mul_f32_e32 v137, 0x42000000, v24
	v_mul_f32_e32 v131, 0x42000000, v28
	v_med3_f32 v136, v137, s28, v149
	v_med3_f32 v131, v131, s28, v149
	v_cvt_pk_fp8_f32 v155, v136, v131 op_sel:[0,0,1]
	v_mul_f32_e32 v131, 0x42000000, v32
	v_mul_f32_e32 v136, 0x42000000, v36
	v_med3_f32 v131, v131, s28, v149
	v_med3_f32 v136, v136, s28, v149
	v_mov_b32_e32 v156, 0
	v_cvt_pk_fp8_f32 v156, v131, v136
	v_mul_f32_e32 v137, 0x42000000, v40
	v_mul_f32_e32 v131, 0x42000000, v44
	v_med3_f32 v136, v137, s28, v149
	v_med3_f32 v131, v131, s28, v149
	v_cvt_pk_fp8_f32 v156, v136, v131 op_sel:[0,0,1]
	v_mul_f32_e32 v131, 0x42000000, v48
	v_mul_f32_e32 v136, 0x42000000, v52
	v_med3_f32 v131, v131, s28, v149
	v_med3_f32 v136, v136, s28, v149
	v_mov_b32_e32 v157, 0
	v_cvt_pk_fp8_f32 v157, v131, v136
	v_mul_f32_e32 v137, 0x42000000, v56
	v_mul_f32_e32 v131, 0x42000000, v60
	v_med3_f32 v136, v137, s28, v149
	v_med3_f32 v131, v131, s28, v149
	v_cvt_pk_fp8_f32 v157, v136, v131 op_sel:[0,0,1]
	v_mul_f32_e32 v131, 0x42000000, v65
	v_mul_f32_e32 v136, 0x42000000, v5
	v_med3_f32 v131, v131, s28, v149
	v_med3_f32 v136, v136, s28, v149
	v_mov_b32_e32 v158, 0
	v_cvt_pk_fp8_f32 v158, v131, v136
	v_mul_f32_e32 v137, 0x42000000, v9
	v_mul_f32_e32 v131, 0x42000000, v13
	v_med3_f32 v136, v137, s28, v149
	v_med3_f32 v131, v131, s28, v149
	v_cvt_pk_fp8_f32 v158, v136, v131 op_sel:[0,0,1]
	v_mul_f32_e32 v131, 0x42000000, v17
	v_mul_f32_e32 v136, 0x42000000, v21
	v_med3_f32 v131, v131, s28, v149
	v_med3_f32 v136, v136, s28, v149
	v_mov_b32_e32 v159, 0
	v_cvt_pk_fp8_f32 v159, v131, v136
	v_mul_f32_e32 v137, 0x42000000, v25
	v_mul_f32_e32 v131, 0x42000000, v29
	v_med3_f32 v136, v137, s28, v149
	v_med3_f32 v131, v131, s28, v149
	v_cvt_pk_fp8_f32 v159, v136, v131 op_sel:[0,0,1]
	v_mul_f32_e32 v131, 0x42000000, v33
	v_mul_f32_e32 v136, 0x42000000, v37
	v_med3_f32 v131, v131, s28, v149
	v_med3_f32 v136, v136, s28, v149
	v_mov_b32_e32 v160, 0
	v_cvt_pk_fp8_f32 v160, v131, v136
	v_mul_f32_e32 v137, 0x42000000, v41
	v_mul_f32_e32 v131, 0x42000000, v45
	v_med3_f32 v136, v137, s28, v149
	v_med3_f32 v131, v131, s28, v149
	v_cvt_pk_fp8_f32 v160, v136, v131 op_sel:[0,0,1]
	v_mul_f32_e32 v131, 0x42000000, v49
	v_mul_f32_e32 v136, 0x42000000, v53
	v_med3_f32 v131, v131, s28, v149
	v_med3_f32 v136, v136, s28, v149
	v_mov_b32_e32 v161, 0
	v_cvt_pk_fp8_f32 v161, v131, v136
	v_mul_f32_e32 v137, 0x42000000, v57
	v_mul_f32_e32 v131, 0x42000000, v61
	v_med3_f32 v136, v137, s28, v149
	v_med3_f32 v131, v131, s28, v149
	v_cvt_pk_fp8_f32 v161, v136, v131 op_sel:[0,0,1]
	s_add_i32 s58, s27, 0xffffff80
	s_cmp_ge_i32 s58, s100
	ds_write_b128 v150, v[132:135] offset:144
	ds_write_b128 v150, v[154:157] offset:288
	ds_write_b128 v150, v[158:161] offset:432
	s_cbranch_scc1 .LBB0_443
	s_cmpk_lt_i32 s58, 0x21c0
	s_cselect_b64 s[6:7], -1, 0
	v_cndmask_b32_e64 v153, 0, 1, s[6:7]
	s_and_b64 s[6:7], s[6:7], exec
	s_cselect_b32 s7, s29, 0xffffde40
	s_movk_i32 s55, 0x800
	s_cselect_b32 s15, 8, 7
	s_cselect_b32 s22, s37, 0x7f
	s_waitcnt lgkmcnt(0)
	s_cselect_b32 s25, s11, s17
	s_cselect_b32 s63, s10, s16
	s_cselect_b32 s65, s30, s33
	s_cselect_b32 s67, s3, s31
	s_cselect_b32 s54, 0x1000, s55
	s_cselect_b32 s23, 23, 22
	s_cselect_b32 s69, 4, 3
	s_cselect_b32 s71, 12, 11
	s_cselect_b32 s64, s38, 0x6000
	s_cselect_b32 s66, s39, 0xa000
	s_cselect_b32 s68, s40, 0xc000
	s_cselect_b32 s70, s41, 0xe000
	s_cselect_b32 s72, s42, 0x12000
	s_cselect_b32 s74, s43, 0x14000
	s_cselect_b32 s76, s44, 0x16000
	s_cselect_b32 s78, s45, 0x18000
	s_cselect_b32 s24, s46, 0x1a000
	s_cselect_b32 s14, s47, 0x1c000
	s_cselect_b32 s6, s48, 0x1e000
	s_add_i32 s7, s7, s27
	s_addk_i32 s7, 0xff80
	s_lshr_b32 s20, s7, s15
	s_and_b32 s7, s7, s22
	s_lshl_b64 s[22:23], s[20:21], s23
	s_lshl_b64 s[56:57], s[22:23], 2
	s_add_u32 s15, s63, s56
	s_addc_u32 s25, s25, s57
	s_add_u32 s22, s67, s22
	s_addc_u32 s23, s65, s23
	s_lshr_b32 s20, s54, 8
	s_lshr_b32 s56, s7, s69
	s_lshl_b32 s56, s56, 7
	s_add_i32 s20, s20, -1
	s_and_b32 s7, s20, s7
	s_add_i32 s20, s56, s26
	s_lshl_b64 s[80:81], s[20:21], s71
	s_lshl_b32 s57, s7, 8
	s_lshl_b64 s[80:81], s[80:81], 2
	s_add_u32 s15, s15, s80
	s_addc_u32 s20, s25, s81
	s_lshl_b32 s7, s7, 10
	s_add_u32 s80, s15, s7
	s_addc_u32 s81, s20, 0
	v_lshlrev_b32_e32 v140, 2, v138
	v_lshl_add_u64 v[58:59], s[80:81], 0, v[140:141]
	s_lshl_b32 s20, s54, 2
	v_lshl_add_u64 v[2:3], v[58:59], 0, s[20:21]
	s_lshl_b32 s20, s54, 3
	v_lshl_add_u64 v[6:7], v[58:59], 0, s[20:21]
	s_lshl_b32 s20, s54, 4
	s_mov_b32 s65, s21
	v_lshl_add_u64 v[14:15], v[58:59], 0, s[20:21]
	s_mov_b32 s67, s21
	s_mov_b32 s69, s21
	s_mov_b32 s71, s21
	s_lshl_b32 s20, s54, 5
	s_mov_b32 s73, s21
	s_mov_b32 s75, s21
	s_mov_b32 s77, s21
	s_mov_b32 s79, s21
	s_mov_b32 s25, s21
	s_mov_b32 s15, s21
	s_mov_b32 s7, s21
	v_lshl_add_u64 v[10:11], v[58:59], 0, s[64:65]
	v_lshl_add_u64 v[18:19], v[58:59], 0, s[66:67]
	v_lshl_add_u64 v[22:23], v[58:59], 0, s[68:69]
	v_lshl_add_u64 v[26:27], v[58:59], 0, s[70:71]
	v_lshl_add_u64 v[30:31], v[58:59], 0, s[20:21]
	v_lshl_add_u64 v[34:35], v[58:59], 0, s[72:73]
	v_lshl_add_u64 v[38:39], v[58:59], 0, s[74:75]
	v_lshl_add_u64 v[42:43], v[58:59], 0, s[76:77]
	v_lshl_add_u64 v[46:47], v[58:59], 0, s[78:79]
	v_lshl_add_u64 v[50:51], v[58:59], 0, s[24:25]
	v_lshl_add_u64 v[54:55], v[58:59], 0, s[14:15]
	v_lshl_add_u64 v[58:59], v[58:59], 0, s[6:7]
	global_load_dwordx4 v[2:5], v[2:3], off nt
	s_nop 0
	global_load_dwordx4 v[6:9], v[6:7], off nt
	s_nop 0
	global_load_dwordx4 v[10:13], v[10:11], off nt
	s_nop 0
	global_load_dwordx4 v[14:17], v[14:15], off nt
	s_nop 0
	global_load_dwordx4 v[18:21], v[18:19], off nt
	s_nop 0
	global_load_dwordx4 v[22:25], v[22:23], off nt
	s_nop 0
	global_load_dwordx4 v[26:29], v[26:27], off nt
	s_nop 0
	global_load_dwordx4 v[30:33], v[30:31], off nt
	s_nop 0
	global_load_dwordx4 v[34:37], v[34:35], off nt
	s_nop 0
	global_load_dwordx4 v[38:41], v[38:39], off nt
	s_nop 0
	global_load_dwordx4 v[42:45], v[42:43], off nt
	s_nop 0
	global_load_dwordx4 v[46:49], v[46:47], off nt
	s_nop 0
	global_load_dwordx4 v[50:53], v[50:51], off nt
	s_nop 0
	global_load_dwordx4 v[54:57], v[54:55], off nt
	s_nop 0
	global_load_dwordx4 v[62:65], v140, s[80:81] nt
	s_nop 0
	global_load_dwordx4 v[58:61], v[58:59], off nt

.LBB0_451:
	v_ashrrev_i32_e32 v137, 31, v134
	v_mad_u64_u32 v[134:135], s[4:5], v134, s61, v[144:145]
	v_mov_b32_e32 v136, v135
	v_mad_u64_u32 v[136:137], s[4:5], v137, s61, v[136:137]
	v_mov_b32_e32 v135, v136
	s_cmp_lt_i32 s27, s98
	s_waitcnt lgkmcnt(0)
	global_store_dwordx4 v[134:135], v[130:133], off nt
	s_cbranch_scc0 .LBB0_439
	s_nop 0
	v_mul_f32_e32 v130, 0x42000000, v122
	v_mul_f32_e32 v131, 0x42000000, v66
	v_med3_f32 v133, v130, s28, v149
	v_med3_f32 v131, v131, s28, v149
	v_mov_b32_e32 v130, 0
	v_cvt_pk_fp8_f32 v130, v133, v131
	v_mul_f32_e32 v132, 0x42000000, v70
	v_mul_f32_e32 v131, 0x42000000, v74
	v_med3_f32 v132, v132, s28, v149
	v_med3_f32 v131, v131, s28, v149
	v_cvt_pk_fp8_f32 v130, v132, v131 op_sel:[0,0,1]
	v_mul_f32_e32 v131, 0x42000000, v78
	v_mul_f32_e32 v132, 0x42000000, v82
	v_med3_f32 v134, v131, s28, v149
	v_med3_f32 v132, v132, s28, v149
	v_mov_b32_e32 v131, 0
	v_cvt_pk_fp8_f32 v131, v134, v132
	v_mul_f32_e32 v133, 0x42000000, v86
	v_mul_f32_e32 v132, 0x42000000, v90
	v_med3_f32 v133, v133, s28, v149
	v_med3_f32 v132, v132, s28, v149
	v_cvt_pk_fp8_f32 v131, v133, v132 op_sel:[0,0,1]
	v_mul_f32_e32 v132, 0x42000000, v94
	v_mul_f32_e32 v133, 0x42000000, v98
	v_med3_f32 v135, v132, s28, v149
	v_med3_f32 v133, v133, s28, v149
	v_mov_b32_e32 v132, 0
	v_cvt_pk_fp8_f32 v132, v135, v133
	v_mul_f32_e32 v134, 0x42000000, v102
	v_mul_f32_e32 v133, 0x42000000, v106
	v_med3_f32 v134, v134, s28, v149
	v_med3_f32 v133, v133, s28, v149
	v_cvt_pk_fp8_f32 v132, v134, v133 op_sel:[0,0,1]
	v_mul_f32_e32 v133, 0x42000000, v110
	v_mul_f32_e32 v134, 0x42000000, v114
	v_med3_f32 v136, v133, s28, v149
	v_med3_f32 v134, v134, s28, v149
	v_mov_b32_e32 v133, 0
	v_cvt_pk_fp8_f32 v133, v136, v134
	v_mul_f32_e32 v135, 0x42000000, v118
	v_mul_f32_e32 v134, 0x42000000, v126
	v_med3_f32 v135, v135, s28, v149
	v_med3_f32 v134, v134, s28, v149
	v_cvt_pk_fp8_f32 v133, v135, v134 op_sel:[0,0,1]
	v_mul_f32_e32 v134, 0x42000000, v123
	v_mul_f32_e32 v135, 0x42000000, v67
	v_med3_f32 v137, v134, s28, v149
	v_med3_f32 v135, v135, s28, v149
	v_mov_b32_e32 v134, 0
	v_cvt_pk_fp8_f32 v134, v137, v135
	v_mul_f32_e32 v136, 0x42000000, v71
	v_mul_f32_e32 v135, 0x42000000, v75
	v_med3_f32 v136, v136, s28, v149
	v_med3_f32 v135, v135, s28, v149
	v_cvt_pk_fp8_f32 v134, v136, v135 op_sel:[0,0,1]
	v_mul_f32_e32 v135, 0x42000000, v79
	v_mul_f32_e32 v136, 0x42000000, v83
	v_med3_f32 v140, v135, s28, v149
	v_med3_f32 v136, v136, s28, v149
	v_mov_b32_e32 v135, 0
	v_cvt_pk_fp8_f32 v135, v140, v136
	v_mul_f32_e32 v137, 0x42000000, v87
	v_mul_f32_e32 v136, 0x42000000, v91
	v_med3_f32 v137, v137, s28, v149
	v_med3_f32 v136, v136, s28, v149
	v_cvt_pk_fp8_f32 v135, v137, v136 op_sel:[0,0,1]
	v_mul_f32_e32 v136, 0x42000000, v95
	v_mul_f32_e32 v137, 0x42000000, v99
	v_med3_f32 v144, v136, s28, v149
	v_med3_f32 v137, v137, s28, v149
	v_mov_b32_e32 v136, 0
	v_cvt_pk_fp8_f32 v136, v144, v137
	v_mul_f32_e32 v140, 0x42000000, v103
	v_mul_f32_e32 v137, 0x42000000, v107
	v_med3_f32 v140, v140, s28, v149
	v_med3_f32 v137, v137, s28, v149
	v_cvt_pk_fp8_f32 v136, v140, v137 op_sel:[0,0,1]
	v_mul_f32_e32 v137, 0x42000000, v111
	v_mul_f32_e32 v140, 0x42000000, v115
	v_med3_f32 v145, v137, s28, v149
	v_med3_f32 v140, v140, s28, v149
	v_mov_b32_e32 v137, 0
	v_cvt_pk_fp8_f32 v137, v145, v140
	v_mul_f32_e32 v144, 0x42000000, v119
	v_mul_f32_e32 v140, 0x42000000, v127
	v_med3_f32 v144, v144, s28, v149
	v_med3_f32 v140, v140, s28, v149
	v_cvt_pk_fp8_f32 v137, v144, v140 op_sel:[0,0,1]
	v_mul_f32_e32 v140, 0x42000000, v124
	v_mul_f32_e32 v144, 0x42000000, v68
	v_med3_f32 v140, v140, s28, v149
	v_med3_f32 v144, v144, s28, v149
	v_mov_b32_e32 v154, 0
	v_cvt_pk_fp8_f32 v154, v140, v144
	v_mul_f32_e32 v145, 0x42000000, v72
	v_mul_f32_e32 v140, 0x42000000, v76
	v_med3_f32 v144, v145, s28, v149
	v_med3_f32 v140, v140, s28, v149
	v_cvt_pk_fp8_f32 v154, v144, v140 op_sel:[0,0,1]
	v_mul_f32_e32 v140, 0x42000000, v80
	v_mul_f32_e32 v144, 0x42000000, v84
	v_med3_f32 v140, v140, s28, v149
	v_med3_f32 v144, v144, s28, v149
	v_mov_b32_e32 v155, 0
	v_cvt_pk_fp8_f32 v155, v140, v144
	v_mul_f32_e32 v145, 0x42000000, v88
	v_mul_f32_e32 v140, 0x42000000, v92
	v_med3_f32 v144, v145, s28, v149
	v_med3_f32 v140, v140, s28, v149
	v_cvt_pk_fp8_f32 v155, v144, v140 op_sel:[0,0,1]
	v_mul_f32_e32 v140, 0x42000000, v96
	v_mul_f32_e32 v144, 0x42000000, v100
	v_med3_f32 v140, v140, s28, v149
	v_med3_f32 v144, v144, s28, v149
	v_mov_b32_e32 v156, 0
	v_cvt_pk_fp8_f32 v156, v140, v144
	v_mul_f32_e32 v145, 0x42000000, v104
	v_mul_f32_e32 v140, 0x42000000, v108
	v_med3_f32 v144, v145, s28, v149
	v_med3_f32 v140, v140, s28, v149
	v_cvt_pk_fp8_f32 v156, v144, v140 op_sel:[0,0,1]
	v_mul_f32_e32 v140, 0x42000000, v112
	v_mul_f32_e32 v144, 0x42000000, v116
	v_med3_f32 v140, v140, s28, v149
	v_med3_f32 v144, v144, s28, v149
	v_mov_b32_e32 v157, 0
	v_cvt_pk_fp8_f32 v157, v140, v144
	v_mul_f32_e32 v145, 0x42000000, v120
	v_mul_f32_e32 v140, 0x42000000, v128
	v_med3_f32 v144, v145, s28, v149
	v_med3_f32 v140, v140, s28, v149
	v_cvt_pk_fp8_f32 v157, v144, v140 op_sel:[0,0,1]
	v_mul_f32_e32 v140, 0x42000000, v125
	v_mul_f32_e32 v144, 0x42000000, v69
	v_med3_f32 v140, v140, s28, v149
	v_med3_f32 v144, v144, s28, v149
	v_mov_b32_e32 v158, 0
	v_cvt_pk_fp8_f32 v158, v140, v144
	v_mul_f32_e32 v145, 0x42000000, v73
	v_mul_f32_e32 v140, 0x42000000, v77
	v_med3_f32 v144, v145, s28, v149
	v_med3_f32 v140, v140, s28, v149
	v_cvt_pk_fp8_f32 v158, v144, v140 op_sel:[0,0,1]
	v_mul_f32_e32 v140, 0x42000000, v81
	v_mul_f32_e32 v144, 0x42000000, v85
	v_med3_f32 v140, v140, s28, v149
	v_med3_f32 v144, v144, s28, v149
	v_mov_b32_e32 v159, 0
	v_cvt_pk_fp8_f32 v159, v140, v144
	v_mul_f32_e32 v145, 0x42000000, v89
	v_mul_f32_e32 v140, 0x42000000, v93
	v_med3_f32 v144, v145, s28, v149
	v_med3_f32 v140, v140, s28, v149
	v_cvt_pk_fp8_f32 v159, v144, v140 op_sel:[0,0,1]
	v_mul_f32_e32 v140, 0x42000000, v97
	v_mul_f32_e32 v144, 0x42000000, v101
	v_med3_f32 v140, v140, s28, v149
	v_med3_f32 v144, v144, s28, v149
	v_mov_b32_e32 v160, 0
	v_cvt_pk_fp8_f32 v160, v140, v144
	v_mul_f32_e32 v145, 0x42000000, v105
	v_mul_f32_e32 v140, 0x42000000, v109
	v_med3_f32 v144, v145, s28, v149
	v_med3_f32 v140, v140, s28, v149
	v_cvt_pk_fp8_f32 v160, v144, v140 op_sel:[0,0,1]
	v_mul_f32_e32 v140, 0x42000000, v113
	v_mul_f32_e32 v144, 0x42000000, v117
	v_med3_f32 v140, v140, s28, v149
	v_med3_f32 v144, v144, s28, v149
	v_mov_b32_e32 v161, 0
	v_cvt_pk_fp8_f32 v161, v140, v144
	v_mul_f32_e32 v145, 0x42000000, v121
	v_mul_f32_e32 v140, 0x42000000, v129
	v_med3_f32 v144, v145, s28, v149
	v_med3_f32 v140, v140, s28, v149
	v_cvt_pk_fp8_f32 v161, v144, v140 op_sel:[0,0,1]
	ds_write_b128 v150, v[130:133] offset:36864
	ds_write_b128 v150, v[134:137] offset:37008
	ds_write_b128 v150, v[154:157] offset:37152
	ds_write_b128 v150, v[158:161] offset:37296
	s_cmp_lt_i32 s27, s100
	s_mov_b32 s65, s36
	s_mov_b32 s66, s53
	v_mov_b32_e32 v154, v1
	s_mov_b32 s63, s49
	s_mov_b32 s64, s52
	s_mov_b64 s[24:25], s[18:19]
	s_cbranch_scc0 .LBB0_454
	s_cmpk_lt_i32 s27, 0x21c0
	s_cselect_b64 s[4:5], -1, 0
	v_cndmask_b32_e64 v154, 0, 1, s[4:5]
	s_and_b64 s[4:5], s[4:5], exec
	s_cselect_b32 s5, s29, 0xffffde40
	s_movk_i32 s64, 0x800
	s_cselect_b32 s7, 8, 7
	s_cselect_b32 s15, s37, 0x7f
	s_cselect_b32 s59, s11, s17
	s_cselect_b32 s61, s10, s16
	s_cselect_b32 s62, s30, s33
	s_cselect_b32 s65, s3, s31
	s_cselect_b32 s63, 0x1000, s64
	s_cselect_b32 s24, 23, 22
	s_cselect_b32 s69, 4, 3
	s_cselect_b32 s71, 12, 11
	s_cselect_b32 s60, s38, 0x6000
	s_cselect_b32 s68, s39, 0xa000
	s_cselect_b32 s70, s40, 0xc000
	s_cselect_b32 s72, s41, 0xe000
	s_cselect_b32 s74, s42, 0x12000
	s_cselect_b32 s76, s43, 0x14000
	s_cselect_b32 s78, s44, 0x16000
	s_cselect_b32 s80, s45, 0x18000
	s_cselect_b32 s14, s46, 0x1a000
	s_cselect_b32 s6, s47, 0x1c000
	s_cselect_b32 s4, s48, 0x1e000
	s_add_i32 s5, s5, s27
	s_lshr_b32 s20, s5, s7
	s_lshl_b64 s[24:25], s[20:21], s24
	s_and_b32 s5, s5, s15
	s_lshl_b64 s[66:67], s[24:25], 2
	s_add_u32 s7, s61, s66
	s_addc_u32 s15, s59, s67
	s_add_u32 s24, s65, s24
	s_addc_u32 s25, s62, s25
	s_lshr_b32 s20, s63, 8
	s_lshr_b32 s59, s5, s69
	s_lshl_b32 s66, s59, 7
	s_add_i32 s20, s20, -1
	s_and_b32 s5, s20, s5
	s_add_i32 s20, s66, s26
	s_lshl_b64 s[82:83], s[20:21], s71
	s_lshl_b32 s65, s5, 8
	s_lshl_b64 s[82:83], s[82:83], 2
	s_add_u32 s7, s7, s82
	s_addc_u32 s15, s15, s83
	s_lshl_b32 s5, s5, 10
	s_add_u32 s82, s7, s5
	s_addc_u32 s83, s15, 0
	v_lshlrev_b32_e32 v140, 2, v138
	v_lshl_add_u64 v[122:123], s[82:83], 0, v[140:141]
	s_lshl_b32 s20, s63, 2
	v_lshl_add_u64 v[66:67], v[122:123], 0, s[20:21]
	s_lshl_b32 s20, s63, 3
	v_lshl_add_u64 v[70:71], v[122:123], 0, s[20:21]
	s_lshl_b32 s20, s63, 4
	s_mov_b32 s61, s21
	v_lshl_add_u64 v[78:79], v[122:123], 0, s[20:21]
	s_mov_b32 s69, s21
	s_mov_b32 s71, s21
	s_mov_b32 s73, s21
	s_lshl_b32 s20, s63, 5
	s_mov_b32 s75, s21
	s_mov_b32 s77, s21
	s_mov_b32 s79, s21
	s_mov_b32 s81, s21
	s_mov_b32 s15, s21
	s_mov_b32 s7, s21
	s_mov_b32 s5, s21
	v_lshl_add_u64 v[74:75], v[122:123], 0, s[60:61]
	v_lshl_add_u64 v[82:83], v[122:123], 0, s[68:69]
	v_lshl_add_u64 v[86:87], v[122:123], 0, s[70:71]
	v_lshl_add_u64 v[90:91], v[122:123], 0, s[72:73]
	v_lshl_add_u64 v[94:95], v[122:123], 0, s[20:21]
	v_lshl_add_u64 v[98:99], v[122:123], 0, s[74:75]
	v_lshl_add_u64 v[102:103], v[122:123], 0, s[76:77]
	v_lshl_add_u64 v[106:107], v[122:123], 0, s[78:79]
	v_lshl_add_u64 v[110:111], v[122:123], 0, s[80:81]
	v_lshl_add_u64 v[114:115], v[122:123], 0, s[14:15]
	v_lshl_add_u64 v[118:119], v[122:123], 0, s[6:7]
	v_lshl_add_u64 v[126:127], v[122:123], 0, s[4:5]
	global_load_dwordx4 v[66:69], v[66:67], off nt
	s_nop 0
	global_load_dwordx4 v[70:73], v[70:71], off nt
	s_nop 0
	global_load_dwordx4 v[74:77], v[74:75], off nt
	s_nop 0
	global_load_dwordx4 v[78:81], v[78:79], off nt
	s_nop 0
	global_load_dwordx4 v[82:85], v[82:83], off nt
	s_nop 0
	global_load_dwordx4 v[86:89], v[86:87], off nt
	s_nop 0
	global_load_dwordx4 v[90:93], v[90:91], off nt
	s_nop 0
	global_load_dwordx4 v[94:97], v[94:95], off nt
	s_nop 0
	global_load_dwordx4 v[98:101], v[98:99], off nt
	s_nop 0
	global_load_dwordx4 v[102:105], v[102:103], off nt
	s_nop 0
	global_load_dwordx4 v[106:109], v[106:107], off nt
	s_nop 0
	global_load_dwordx4 v[110:113], v[110:111], off nt
	s_nop 0
	global_load_dwordx4 v[114:117], v[114:115], off nt
	s_nop 0
	global_load_dwordx4 v[118:121], v[118:119], off nt
	s_nop 0
	global_load_dwordx4 v[122:125], v140, s[82:83] nt
	s_nop 0
	global_load_dwordx4 v[126:129], v[126:127], off nt

.LBB0_462:
	s_nop 0
	v_mad_u64_u32 v[134:135], s[4:5], v1, s52, v[144:145]
	s_addk_i32 s27, 0x100
	v_ashrrev_i32_e32 v137, 31, v1
	v_mov_b32_e32 v136, v135
	v_mad_u64_u32 v[136:137], s[4:5], v137, s52, v[136:137]
	s_cmp_ge_i32 s58, s100
	v_mov_b32_e32 v135, v136
	s_cselect_b64 s[4:5], -1, 0
	s_waitcnt lgkmcnt(0)
	global_store_dwordx4 v[134:135], v[130:133], off nt
	s_branch .LBB0_440

; #define PG8_WAIT_V(n) asm volatile("s_waitcnt vmcnt(" #n ")" ::: "memory")
; #define PG8_BAR __builtin_amdgcn_s_barrier()
;     ...
;     PG8_WAIT_V(0);
;     PG8_BAR;
; __global__ void __launch_bounds__(NWAVES * 64, 2) fwd_kernel(Args args) {
;     ...
;         const bool split2 = (G == 256); const int xcd2 = bx & 7, slot2 = bx >> 3;
;         if (!split2 || slot2 < T8_GS) {
;         SchedDense S; S.init(Z_FP8 ? (const void*)XN8 : (const void*)XN, WinT, T, INW, D, D, split2 ? T8_GS * 8 : G, split2 ? slot2 * 8 + xcd2 : bx, Z_FP8 ? 1 : 2);
;         EpiZ E{UP, UG, SGP, SGS, Z_FP8 ? 0.03125f : 1.0f};
;         pg8::gemm_phase<EpiZ, SchedDense, false, Z_FP8 ? 1 : 2>(lds + RING_OFF, D, D, D, S, E);
;         } else { constexpr int TRB = 256 * 144; T8_CONSTS; T8_RUN(U_TOT - T8_NMOVE + (slot2 - T8_GS) * 8 + xcd2, (32 - T8_GS) * 8, U_TOT); }
.LBB0_560:
	s_waitcnt vmcnt(0)
	s_barrier
	v_readlane_b32 s4, v254, 1
	v_readlane_b32 s5, v254, 2
	s_movk_i32 s98, 0x32c0
	s_movk_i32 s99, 0x3240
	s_movk_i32 s100, 0x31c0
	s_movk_i32 s101, 0x2fc0
	s_load_dwordx2 s[8:9], s[4:5], 0xf8
	s_branch .Lp2_conv_entry

;     __device__ __forceinline__ unsigned a_rowoff(const Unit& u, int r) const { const int idx = (r < u.nvalid) ? (u.rb * 256 + r) : 0; const int tok = ltok[(size_t)u.e * LCAP + idx]; return (unsigned)tok * (unsigned)D; }
;     __device__ __forceinline__ int krot(const Unit& u, int nt) const { return (2 * u.rb + u.pn) % nt; }
;     ...
;         rotn = has_next ? S.krot(nxt, nt) : rotc;
;         const bool full = !HALFU || cur.nvalid > 128;
; #pragma unroll 1
;         for (int t = 0; t < nt; t += 2) {
;             const bool last = (t == nt - 2);
;             const bool fin = last && !has_next;
;             const char* a1 = cA + PG8_KOFS(rotc, t + 1);
;             const size_t k2 = last ? PG8_KOFS(rotn, 0) : PG8_KOFS(rotc, t + 2), k3 = last ? PG8_KOFS(rotn, 1) : PG8_KOFS(rotc, t + 3);
;             const char* a2 = (last ? nA : cA) + k2; const char* b2 = (last ? nB : cB) + k2;
;             const char* a3 = (last ? nA : cA) + k3; const char* b3 = (last ? nB : cB) + k3;
;             unsigned o2[2][2];
; #pragma unroll
;             for (int h = 0; h < 2; ++h)
; #pragma unroll
;                 for (int i = 0; i < 2; ++i) o2[h][i] = gcur[h][i];
;             if constexpr (GATHER) {
;                 if (t == 0 && has_next) {
; #pragma unroll
;                     for (int h = 0; h < 2; ++h)
; #pragma unroll
;                         for (int i = 0; i < 2; ++i) gnxt[h][i] = S.a_rowoff(nxt, h * HALF + rowA[i]) + colA[i];
;                 }
;                 if (last && has_next) {
;                     asm volatile("" : "+v"(gnxt[0][0]), "+v"(gnxt[0][1]), "+v"(gnxt[1][0]), "+v"(gnxt[1][1]));
; #pragma unroll
;                     for (int h = 0; h < 2; ++h)
; #pragma unroll
;                         for (int i = 0; i < 2; ++i) o2[h][i] = gnxt[h][i];
;                 }
;             }
;     ...
; #pragma unroll
;         for (int a = 0; a < 2; ++a)
; #pragma unroll
;             for (int b = 0; b < 2; ++b)
; #pragma unroll
;                 for (int m = 0; m < 4; ++m)
; #pragma unroll
;                     for (int n = 0; n < 2; ++n) acc[a][b][m][n] = (f32x4){0.f, 0.f, 0.f, 0.f};
;         cur = nxt; cA = nA; cB = nB; rotc = rotn; ++ui;
; #pragma unroll
;         for (int h = 0; h < 2; ++h)
; #pragma unroll
;             for (int i = 0; i < 2; ++i) gcur[h][i] = gnxt[h][i];
.LBB0_1307:
	s_lshl_b32 s8, s78, 1
	s_add_i32 s8, s24, s8
	s_ashr_i32 s9, s8, 31
	s_lshr_b32 s9, s9, 28
	s_add_i32 s9, s8, s9
	s_and_b32 s9, s9, -16
	s_sub_i32 s25, s8, s9
	s_and_b64 s[8:9], s[40:41], exec
	s_cselect_b32 s42, s25, s38
	s_cmpk_gt_i32 s10, 0x80
	s_cselect_b64 s[44:45], -1, 0
	s_ashr_i32 s43, s42, 31
	s_xor_b64 s[46:47], s[40:41], -1
	s_lshl_b64 s[8:9], s[42:43], 7
	s_add_u32 s8, s8, 0x80
	s_addc_u32 s9, s9, 0
	s_cmp_lt_i32 s42, 15
	s_cselect_b32 s29, s9, 0
	s_cselect_b32 s43, s8, 0
	s_lshl_b32 s10, s78, 8
	v_or_b32_e32 v2, s10, v1
	v_cmp_gt_i32_e32 vcc, s79, v1
	v_or_b32_e32 v4, s10, v195
	v_or_b32_e32 v6, s10, v216
	v_cndmask_b32_e32 v2, 0, v2, vcc
	v_cmp_gt_i32_e32 vcc, s79, v195
	s_lshl_b64 s[8:9], s[22:23], 16
	v_or_b32_e32 v8, s10, v217
	v_cndmask_b32_e32 v4, 0, v4, vcc
	v_cmp_gt_i32_e32 vcc, s79, v216
	s_add_u32 s8, s49, s8
	v_mov_b32_e32 v68, v201
	v_cndmask_b32_e32 v6, 0, v6, vcc
	v_cmp_gt_i32_e32 vcc, s79, v217
	v_mov_b32_e32 v69, v201
	v_ashrrev_i32_e32 v3, 31, v2
	v_cndmask_b32_e32 v8, 0, v8, vcc
	v_ashrrev_i32_e32 v5, 31, v4
	v_ashrrev_i32_e32 v7, 31, v6
	v_ashrrev_i32_e32 v9, 31, v8
	s_addc_u32 s9, s58, s9
	v_mov_b32_e32 v66, v201
	v_mov_b32_e32 v67, v201
	v_mov_b32_e32 v130, 0
	v_mov_b64_e32 v[72:73], v[68:69]
	v_mov_b64_e32 v[84:85], v[68:69]
	v_mov_b64_e32 v[88:89], v[68:69]
	v_mov_b64_e32 v[100:101], v[68:69]
	v_mov_b64_e32 v[104:105], v[68:69]
	v_mov_b64_e32 v[116:117], v[68:69]
	v_mov_b64_e32 v[120:121], v[68:69]
	v_mov_b64_e32 v[76:77], v[68:69]
	v_mov_b64_e32 v[80:81], v[68:69]
	v_mov_b64_e32 v[92:93], v[68:69]
	v_mov_b64_e32 v[96:97], v[68:69]
	v_mov_b64_e32 v[108:109], v[68:69]
	v_mov_b64_e32 v[112:113], v[68:69]
	v_mov_b64_e32 v[124:125], v[68:69]
	v_mov_b64_e32 v[128:129], v[68:69]
	v_mov_b32_e32 v203, v201
	v_lshl_add_u64 v[208:209], v[2:3], 2, s[8:9]
	v_lshl_add_u64 v[210:211], v[4:5], 2, s[8:9]
	v_lshl_add_u64 v[212:213], v[6:7], 2, s[8:9]
	v_lshl_add_u64 v[214:215], v[8:9], 2, s[8:9]
	s_mov_b32 s23, -2
	v_mov_b64_e32 v[70:71], v[66:67]
	v_mov_b64_e32 v[82:83], v[66:67]
	v_mov_b64_e32 v[86:87], v[66:67]
	v_mov_b64_e32 v[98:99], v[66:67]
	v_mov_b64_e32 v[102:103], v[66:67]
	v_mov_b64_e32 v[114:115], v[66:67]
	v_mov_b64_e32 v[118:119], v[66:67]
	v_mov_b64_e32 v[74:75], v[66:67]
	v_mov_b64_e32 v[78:79], v[66:67]
	v_mov_b64_e32 v[90:91], v[66:67]
	v_mov_b64_e32 v[94:95], v[66:67]
	v_mov_b64_e32 v[106:107], v[66:67]
	v_mov_b64_e32 v[110:111], v[66:67]
	v_mov_b64_e32 v[122:123], v[66:67]
	v_mov_b64_e32 v[126:127], v[66:67]
	v_mov_b32_e32 v230, v202
	v_mov_b32_e32 v229, v200
	v_mov_b32_e32 v228, v204
	v_mov_b32_e32 v227, v206
	v_mov_b32_e32 v131, v130
	v_mov_b32_e32 v132, v130
	v_mov_b32_e32 v133, v130
	v_mov_b32_e32 v134, v130
	v_mov_b32_e32 v135, v130
	v_mov_b32_e32 v136, v130
	v_mov_b32_e32 v137, v130
	v_mov_b32_e32 v146, v130
	v_mov_b32_e32 v147, v130
	v_mov_b32_e32 v148, v130
	v_mov_b32_e32 v149, v130
	v_mov_b32_e32 v150, v130
	v_mov_b32_e32 v151, v130
	v_mov_b32_e32 v152, v130
	v_mov_b32_e32 v153, v130
	v_mov_b32_e32 v162, v130
	v_mov_b32_e32 v163, v130
	v_mov_b32_e32 v164, v130
	v_mov_b32_e32 v165, v130
	v_mov_b32_e32 v166, v130
	v_mov_b32_e32 v167, v130
	v_mov_b32_e32 v168, v130
	v_mov_b32_e32 v169, v130
	v_mov_b32_e32 v178, v130
	v_mov_b32_e32 v179, v130
	v_mov_b32_e32 v180, v130
	v_mov_b32_e32 v181, v130
	v_mov_b32_e32 v182, v130
	v_mov_b32_e32 v183, v130
	v_mov_b32_e32 v184, v130
	v_mov_b32_e32 v185, v130
	v_mov_b32_e32 v138, v130
	v_mov_b32_e32 v139, v130
	v_mov_b32_e32 v140, v130
	v_mov_b32_e32 v141, v130
	v_mov_b32_e32 v142, v130
	v_mov_b32_e32 v143, v130
	v_mov_b32_e32 v144, v130
	v_mov_b32_e32 v145, v130
	v_mov_b32_e32 v154, v130
	v_mov_b32_e32 v155, v130
	v_mov_b32_e32 v156, v130
	v_mov_b32_e32 v157, v130
	v_mov_b32_e32 v158, v130
	v_mov_b32_e32 v159, v130
	v_mov_b32_e32 v160, v130
	v_mov_b32_e32 v161, v130
	v_mov_b32_e32 v170, v130
	v_mov_b32_e32 v171, v130
	v_mov_b32_e32 v172, v130
	v_mov_b32_e32 v173, v130
	v_mov_b32_e32 v174, v130
	v_mov_b32_e32 v175, v130
	v_mov_b32_e32 v176, v130
	v_mov_b32_e32 v177, v130
	v_mov_b32_e32 v186, v130
	v_mov_b32_e32 v187, v130
	v_mov_b32_e32 v188, v130
	v_mov_b32_e32 v189, v130
	v_mov_b32_e32 v190, v130
	v_mov_b32_e32 v191, v130
	v_mov_b32_e32 v192, v130
	v_mov_b32_e32 v193, v130
	s_and_b64 vcc, exec, s[44:45]
	s_cbranch_vccz .LBB0_1309
	s_and_b64 vcc, exec, s[40:41]
	s_cbranch_vccz .Lp9_nognxt
	global_load_dword v227, v[208:209], off
	global_load_dword v228, v[210:211], off
	global_load_dword v229, v[212:213], off
	global_load_dword v230, v[214:215], off
.Lp9_nognxt:
	v_add_u32_e32 v238, 0x10000, v223
	v_add_u32_e32 v239, 0x14000, v223
	v_add_u32_e32 v240, 0x18000, v223
	v_add_u32_e32 v241, 0x1c000, v223
; #define PG8_STAGE2(bufoff, gbase, o0, o1) do { \
;         __builtin_amdgcn_global_load_lds((const unsigned*)((const char*)(gbase) + (o0)), (PG8_LAS unsigned*)(lds + (bufoff) + ldsw), 16, 0, 0); \
;         __builtin_amdgcn_global_load_lds((const unsigned*)((const char*)(gbase) + (o1)), (PG8_LAS unsigned*)(lds + (bufoff) + ldsw + 8192), 16, 0, 0); } while (0)
; #define PG8_STAGE_B(bufoff, gbase) PG8_STAGE2(bufoff, gbase, voffB[0], voffB[1])
; #define PG8_WAIT_V(n) asm volatile("s_waitcnt vmcnt(" #n ")" ::: "memory")
; #define PG8_WAIT_L(n) asm volatile("s_waitcnt lgkmcnt(" #n ")" ::: "memory")
; #define PG8_BAR __builtin_amdgcn_s_barrier()
; #define PG8_SCHED __builtin_amdgcn_sched_barrier(0)
;     ...
;             PG8_LDB(B0, 0, 0); PG8_LDB(B1, 0, 1); PG8_SCHED; PG8_LDA(At, 0, 0); PG8_STAGE2(PG8_SA(1, 1), a1 + hstepA, gcur[1][0], gcur[1][1]);
;             PG8_WAIT_V(8); PG8_WAIT_L(0); PG8_BAR; PG8_MMA(0, 0, At, B0); PG8_MMA(0, 1, At, B1); PG8_BAR; PG8_SCHED;
;             if (full) { PG8_LDA(At, 0, 1); }
;             if (!fin) { PG8_STAGE_B(PG8_SB(0, 0), b2); PG8_STAGE_B(PG8_SB(0, 1), b2 + hstepB); PG8_STAGE2(PG8_SA(0, 0), a2, o2[0][0], o2[0][1]); PG8_WAIT_V(8); }
;             else { PG8_WAIT_V(2); }
;             PG8_WAIT_L(0); PG8_BAR; if (full) { PG8_MMA(1, 0, At, B0); PG8_MMA(1, 1, At, B1); } PG8_BAR; PG8_SCHED;
.Lp9_top:
	s_add_i32 s82, s38, s23
	s_add_i32 s84, s82, 3
	s_and_b32 s84, s84, 15
	s_lshl_b32 s84, s84, 7
	s_add_u32 s8, s59, s84
	s_addc_u32 s9, s60, 0
	ds_read_b128 v[10:13], v238
	ds_read_b128 v[14:17], v238 offset:1024
	ds_read_b128 v[26:29], v238 offset:2048
	ds_read_b128 v[30:33], v238 offset:3072
	ds_read_b128 v[2:5], v239
	ds_read_b128 v[6:9], v239 offset:1024
	ds_read_b128 v[18:21], v239 offset:2048
	ds_read_b128 v[22:25], v239 offset:3072
	ds_read_b128 v[34:37], v224
	ds_read_b128 v[38:41], v224 offset:1024
	ds_read_b128 v[42:45], v224 offset:2048
	ds_read_b128 v[46:49], v224 offset:3072
	ds_read_b128 v[50:53], v224 offset:4096
	ds_read_b128 v[54:57], v224 offset:5120
	ds_read_b128 v[58:61], v224 offset:6144
	ds_read_b128 v[62:65], v224 offset:7168
	s_add_i32 m0, s31, 0xc000
	s_nop 0
	global_load_lds_dwordx4 v200, s[8:9]
	s_add_i32 m0, s31, 0xe000
	s_nop 0
	global_load_lds_dwordx4 v202, s[8:9]
	s_waitcnt vmcnt(8)
	s_waitcnt lgkmcnt(0)
	s_barrier
	s_setprio 1
	s_nop 1
	v_mfma_f32_16x16x128_f8f6f4 v[190:193], v[10:17], v[34:41], v[190:193]
	v_mfma_f32_16x16x128_f8f6f4 v[186:189], v[26:33], v[34:41], v[186:189]
	v_mfma_f32_16x16x128_f8f6f4 v[174:177], v[10:17], v[42:49], v[174:177]
	v_mfma_f32_16x16x128_f8f6f4 v[170:173], v[26:33], v[42:49], v[170:173]
	v_mfma_f32_16x16x128_f8f6f4 v[158:161], v[10:17], v[50:57], v[158:161]
	v_mfma_f32_16x16x128_f8f6f4 v[154:157], v[26:33], v[50:57], v[154:157]
	v_mfma_f32_16x16x128_f8f6f4 v[142:145], v[10:17], v[58:65], v[142:145]
	v_mfma_f32_16x16x128_f8f6f4 v[138:141], v[26:33], v[58:65], v[138:141]
	v_mfma_f32_16x16x128_f8f6f4 v[182:185], v[2:9], v[34:41], v[182:185]
	v_mfma_f32_16x16x128_f8f6f4 v[178:181], v[18:25], v[34:41], v[178:181]
	v_mfma_f32_16x16x128_f8f6f4 v[166:169], v[2:9], v[42:49], v[166:169]
	v_mfma_f32_16x16x128_f8f6f4 v[162:165], v[18:25], v[42:49], v[162:165]
	v_mfma_f32_16x16x128_f8f6f4 v[150:153], v[2:9], v[50:57], v[150:153]
	v_mfma_f32_16x16x128_f8f6f4 v[146:149], v[18:25], v[50:57], v[146:149]
	v_mfma_f32_16x16x128_f8f6f4 v[134:137], v[2:9], v[58:65], v[134:137]
	v_mfma_f32_16x16x128_f8f6f4 v[130:133], v[18:25], v[58:65], v[130:133]
	s_setprio 0
	s_barrier
	s_add_i32 s84, s82, 4
	s_and_b32 s84, s84, 15
	s_lshl_b32 s84, s84, 7
	ds_read_b128 v[34:37], v224 offset:16384
	ds_read_b128 v[38:41], v224 offset:17408
	ds_read_b128 v[42:45], v224 offset:18432
	ds_read_b128 v[46:49], v224 offset:19456
	ds_read_b128 v[50:53], v224 offset:20480
	ds_read_b128 v[54:57], v224 offset:21504
	ds_read_b128 v[58:61], v224 offset:22528
	ds_read_b128 v[62:65], v224 offset:23552
	s_add_u32 s52, s36, s84
	s_addc_u32 s53, s37, 0
	s_add_u32 s56, s52, 0x40000
	s_addc_u32 s57, s53, 0
	s_add_u32 s14, s59, s84
	s_addc_u32 s15, s60, 0
	s_mov_b32 m0, s39
	s_nop 0
	global_load_lds_dwordx4 v196, s[52:53]
	s_mov_b32 m0, s61
	s_nop 0
	global_load_lds_dwordx4 v198, s[52:53]
	s_mov_b32 m0, s62
	s_nop 0
	global_load_lds_dwordx4 v196, s[56:57]
	s_mov_b32 m0, s63
	s_nop 0
	global_load_lds_dwordx4 v198, s[56:57]
	s_mov_b32 m0, s31
	s_nop 0
	global_load_lds_dwordx4 v206, s[14:15]
	s_mov_b32 m0, s64
	s_nop 0
	global_load_lds_dwordx4 v204, s[14:15]
	s_waitcnt vmcnt(8)
	s_waitcnt lgkmcnt(0)
	s_barrier
	s_setprio 1
	s_nop 1
	v_mfma_f32_16x16x128_f8f6f4 v[126:129], v[10:17], v[34:41], v[126:129]
	v_mfma_f32_16x16x128_f8f6f4 v[122:125], v[26:33], v[34:41], v[122:125]
	v_mfma_f32_16x16x128_f8f6f4 v[110:113], v[10:17], v[42:49], v[110:113]
	v_mfma_f32_16x16x128_f8f6f4 v[106:109], v[26:33], v[42:49], v[106:109]
	v_mfma_f32_16x16x128_f8f6f4 v[94:97], v[10:17], v[50:57], v[94:97]
	v_mfma_f32_16x16x128_f8f6f4 v[90:93], v[26:33], v[50:57], v[90:93]
	v_mfma_f32_16x16x128_f8f6f4 v[78:81], v[10:17], v[58:65], v[78:81]
	v_mfma_f32_16x16x128_f8f6f4 v[74:77], v[26:33], v[58:65], v[74:77]
	v_mfma_f32_16x16x128_f8f6f4 v[118:121], v[2:9], v[34:41], v[118:121]
	v_mfma_f32_16x16x128_f8f6f4 v[114:117], v[18:25], v[34:41], v[114:117]
	v_mfma_f32_16x16x128_f8f6f4 v[102:105], v[2:9], v[42:49], v[102:105]
	v_mfma_f32_16x16x128_f8f6f4 v[98:101], v[18:25], v[42:49], v[98:101]
	v_mfma_f32_16x16x128_f8f6f4 v[86:89], v[2:9], v[50:57], v[86:89]
	v_mfma_f32_16x16x128_f8f6f4 v[82:85], v[18:25], v[50:57], v[82:85]
	v_mfma_f32_16x16x128_f8f6f4 v[70:73], v[2:9], v[58:65], v[70:73]
	v_mfma_f32_16x16x128_f8f6f4 v[66:69], v[18:25], v[58:65], v[66:69]
	s_setprio 0
	s_barrier
; #define PG8_STAGE2(bufoff, gbase, o0, o1) do { \
;         __builtin_amdgcn_global_load_lds((const unsigned*)((const char*)(gbase) + (o0)), (PG8_LAS unsigned*)(lds + (bufoff) + ldsw), 16, 0, 0); \
;         __builtin_amdgcn_global_load_lds((const unsigned*)((const char*)(gbase) + (o1)), (PG8_LAS unsigned*)(lds + (bufoff) + ldsw + 8192), 16, 0, 0); } while (0)
; #define PG8_STAGE_B(bufoff, gbase) PG8_STAGE2(bufoff, gbase, voffB[0], voffB[1])
; #define PG8_WAIT_V(n) asm volatile("s_waitcnt vmcnt(" #n ")" ::: "memory")
; #define PG8_WAIT_L(n) asm volatile("s_waitcnt lgkmcnt(" #n ")" ::: "memory")
; #define PG8_BAR __builtin_amdgcn_s_barrier()
; #define PG8_SCHED __builtin_amdgcn_sched_barrier(0)
;     ...
;             PG8_LDB(B0, 1, 0); PG8_LDB(B1, 1, 1); PG8_SCHED; PG8_LDA(At, 1, 0);
;             if (!fin) { PG8_STAGE2(PG8_SA(0, 1), a2 + hstepA, o2[1][0], o2[1][1]); PG8_WAIT_V(8); } else { PG8_WAIT_V(0); }
;             PG8_WAIT_L(0); PG8_BAR; PG8_MMA(0, 0, At, B0); PG8_MMA(0, 1, At, B1); PG8_BAR; PG8_SCHED;
;             if (full) { PG8_LDA(At, 1, 1); }
;             if (!fin) { PG8_STAGE_B(PG8_SB(1, 0), b3); PG8_STAGE_B(PG8_SB(1, 1), b3 + hstepB); PG8_STAGE2(PG8_SA(1, 0), a3, o2[0][0], o2[0][1]); PG8_WAIT_V(8); }
;             PG8_WAIT_L(0); PG8_BAR; if (full) { PG8_MMA(1, 0, At, B0); PG8_MMA(1, 1, At, B1); } PG8_BAR; PG8_SCHED;
;         }
	s_add_i32 s84, s82, 5
	s_and_b32 s84, s84, 15
	s_lshl_b32 s84, s84, 7
	ds_read_b128 v[50:53], v240
	ds_read_b128 v[54:57], v240 offset:1024
	ds_read_b128 v[58:61], v240 offset:2048
	ds_read_b128 v[62:65], v240 offset:3072
	ds_read_b128 v[2:5], v241
	ds_read_b128 v[6:9], v241 offset:1024
	ds_read_b128 v[10:13], v241 offset:2048
	ds_read_b128 v[14:17], v241 offset:3072
	ds_read_b128 v[18:21], v224 offset:32768
	ds_read_b128 v[22:25], v224 offset:33792
	ds_read_b128 v[26:29], v224 offset:34816
	ds_read_b128 v[30:33], v224 offset:35840
	ds_read_b128 v[34:37], v224 offset:36864
	ds_read_b128 v[38:41], v224 offset:37888
	ds_read_b128 v[42:45], v224 offset:38912
	ds_read_b128 v[46:49], v224 offset:39936
	s_mov_b32 m0, s65
	s_nop 0
	global_load_lds_dwordx4 v200, s[14:15]
	s_mov_b32 m0, s66
	s_nop 0
	global_load_lds_dwordx4 v202, s[14:15]
	s_waitcnt vmcnt(8)
	s_waitcnt lgkmcnt(0)
	s_barrier
	s_setprio 1
	s_nop 1
	v_mfma_f32_16x16x128_f8f6f4 v[190:193], v[50:57], v[18:25], v[190:193]
	v_mfma_f32_16x16x128_f8f6f4 v[186:189], v[58:65], v[18:25], v[186:189]
	v_mfma_f32_16x16x128_f8f6f4 v[174:177], v[50:57], v[26:33], v[174:177]
	v_mfma_f32_16x16x128_f8f6f4 v[170:173], v[58:65], v[26:33], v[170:173]
	v_mfma_f32_16x16x128_f8f6f4 v[158:161], v[50:57], v[34:41], v[158:161]
	v_mfma_f32_16x16x128_f8f6f4 v[154:157], v[58:65], v[34:41], v[154:157]
	v_mfma_f32_16x16x128_f8f6f4 v[142:145], v[50:57], v[42:49], v[142:145]
	v_mfma_f32_16x16x128_f8f6f4 v[138:141], v[58:65], v[42:49], v[138:141]
	v_mfma_f32_16x16x128_f8f6f4 v[182:185], v[2:9], v[18:25], v[182:185]
	v_mfma_f32_16x16x128_f8f6f4 v[178:181], v[10:17], v[18:25], v[178:181]
	v_mfma_f32_16x16x128_f8f6f4 v[166:169], v[2:9], v[26:33], v[166:169]
	v_mfma_f32_16x16x128_f8f6f4 v[162:165], v[10:17], v[26:33], v[162:165]
	v_mfma_f32_16x16x128_f8f6f4 v[150:153], v[2:9], v[34:41], v[150:153]
	v_mfma_f32_16x16x128_f8f6f4 v[146:149], v[10:17], v[34:41], v[146:149]
	v_mfma_f32_16x16x128_f8f6f4 v[134:137], v[2:9], v[42:49], v[134:137]
	v_mfma_f32_16x16x128_f8f6f4 v[130:133], v[10:17], v[42:49], v[130:133]
	s_setprio 0
	s_barrier
	ds_read_b128 v[18:21], v224 offset:49152
	ds_read_b128 v[22:25], v224 offset:50176
	ds_read_b128 v[26:29], v224 offset:51200
	ds_read_b128 v[30:33], v224 offset:52224
	ds_read_b128 v[34:37], v224 offset:53248
	ds_read_b128 v[38:41], v224 offset:54272
	ds_read_b128 v[42:45], v224 offset:55296
	ds_read_b128 v[46:49], v224 offset:56320
	s_add_u32 s10, s36, s84
	s_addc_u32 s11, s37, 0
	s_add_u32 s34, s10, 0x40000
	s_addc_u32 s35, s11, 0
	s_add_u32 s90, s59, s84
	s_addc_u32 s91, s60, 0
	s_mov_b32 m0, s70
	s_nop 0
	global_load_lds_dwordx4 v196, s[10:11]
	s_mov_b32 m0, s71
	s_nop 0
	global_load_lds_dwordx4 v198, s[10:11]
	s_mov_b32 m0, s74
	s_nop 0
	global_load_lds_dwordx4 v196, s[34:35]
	s_mov_b32 m0, s75
	s_nop 0
	global_load_lds_dwordx4 v198, s[34:35]
	s_mov_b32 m0, s72
	s_nop 0
	global_load_lds_dwordx4 v206, s[90:91]
	s_mov_b32 m0, s73
	s_nop 0
	global_load_lds_dwordx4 v204, s[90:91]
	s_waitcnt vmcnt(8)
	s_waitcnt lgkmcnt(0)
	s_barrier
	s_setprio 1
	s_nop 1
	v_mfma_f32_16x16x128_f8f6f4 v[126:129], v[50:57], v[18:25], v[126:129]
	v_mfma_f32_16x16x128_f8f6f4 v[122:125], v[58:65], v[18:25], v[122:125]
	v_mfma_f32_16x16x128_f8f6f4 v[110:113], v[50:57], v[26:33], v[110:113]
	v_mfma_f32_16x16x128_f8f6f4 v[106:109], v[58:65], v[26:33], v[106:109]
	v_mfma_f32_16x16x128_f8f6f4 v[94:97], v[50:57], v[34:41], v[94:97]
	v_mfma_f32_16x16x128_f8f6f4 v[90:93], v[58:65], v[34:41], v[90:93]
	v_mfma_f32_16x16x128_f8f6f4 v[78:81], v[50:57], v[42:49], v[78:81]
	v_mfma_f32_16x16x128_f8f6f4 v[74:77], v[58:65], v[42:49], v[74:77]
	v_mfma_f32_16x16x128_f8f6f4 v[118:121], v[2:9], v[18:25], v[118:121]
	v_mfma_f32_16x16x128_f8f6f4 v[114:117], v[10:17], v[18:25], v[114:117]
	v_mfma_f32_16x16x128_f8f6f4 v[102:105], v[2:9], v[26:33], v[102:105]
	v_mfma_f32_16x16x128_f8f6f4 v[98:101], v[10:17], v[26:33], v[98:101]
	v_mfma_f32_16x16x128_f8f6f4 v[86:89], v[2:9], v[34:41], v[86:89]
	v_mfma_f32_16x16x128_f8f6f4 v[82:85], v[10:17], v[34:41], v[82:85]
	v_mfma_f32_16x16x128_f8f6f4 v[70:73], v[2:9], v[42:49], v[70:73]
	v_mfma_f32_16x16x128_f8f6f4 v[66:69], v[10:17], v[42:49], v[66:69]
	s_setprio 0
	s_barrier
	s_add_i32 s23, s23, 2
	s_cmp_lt_i32 s23, 12
	s_cbranch_scc1 .Lp9_top
	s_and_b64 vcc, exec, s[40:41]
	s_cbranch_vccz .LBB0_1309
	s_waitcnt vmcnt(8)
	v_lshl_or_b32 v227, v227, 11, v218
	v_lshl_or_b32 v228, v228, 11, v218
	v_lshl_or_b32 v229, v229, 11, v218
	v_lshl_or_b32 v230, v230, 11, v218
	s_branch .LBB0_1309

; __global__ void __launch_bounds__(NWAVES * 64, 2) fwd_kernel(Args args) {
	.amdhsa_kernel _Z10fwd_kernel4Args
		.amdhsa_group_segment_fixed_size 0
		.amdhsa_private_segment_fixed_size 0
		.amdhsa_kernarg_size 528
		.amdhsa_user_sgpr_count 2
		.amdhsa_user_sgpr_dispatch_ptr 0
		.amdhsa_user_sgpr_queue_ptr 0
		.amdhsa_user_sgpr_kernarg_segment_ptr 1
		.amdhsa_user_sgpr_dispatch_id 0
		.amdhsa_user_sgpr_kernarg_preload_length 0
		.amdhsa_user_sgpr_kernarg_preload_offset 0
		.amdhsa_user_sgpr_private_segment_size 0
		.amdhsa_uses_dynamic_stack 0
		.amdhsa_enable_private_segment 0
		.amdhsa_system_sgpr_workgroup_id_x 1
		.amdhsa_system_sgpr_workgroup_id_y 0
		.amdhsa_system_sgpr_workgroup_id_z 0
		.amdhsa_system_sgpr_workgroup_info 0
		.amdhsa_system_vgpr_workitem_id 0
		.amdhsa_next_free_vgpr 255
		.amdhsa_next_free_sgpr 102
		.amdhsa_accum_offset 256
		.amdhsa_reserve_vcc 1
		.amdhsa_float_round_mode_32 0
		.amdhsa_float_round_mode_16_64 0
		.amdhsa_float_denorm_mode_32 3
		.amdhsa_float_denorm_mode_16_64 3
		.amdhsa_dx10_clamp 1
		.amdhsa_ieee_mode 1
		.amdhsa_fp16_overflow 0
		.amdhsa_tg_split 0
		.amdhsa_exception_fp_ieee_invalid_op 0
		.amdhsa_exception_fp_denorm_src 0
		.amdhsa_exception_fp_ieee_div_zero 0
		.amdhsa_exception_fp_ieee_overflow 0
		.amdhsa_exception_fp_ieee_underflow 0
		.amdhsa_exception_fp_ieee_inexact 0
		.amdhsa_exception_int_div_zero 0
	.end_amdhsa_kernel

; __global__ void __launch_bounds__(NWAVES * 64, 2) fwd_kernel(Args args) {
amdhsa.kernels:
  - .agpr_count:     0
    .args:
      - .offset:         0
        .size:           272
        .value_kind:     by_value
      - .offset:         272
        .size:           4
        .value_kind:     hidden_block_count_x
      - .offset:         276
        .size:           4
        .value_kind:     hidden_block_count_y
      - .offset:         280
        .size:           4
        .value_kind:     hidden_block_count_z
      - .offset:         284
        .size:           2
        .value_kind:     hidden_group_size_x
      - .offset:         286
        .size:           2
        .value_kind:     hidden_group_size_y
      - .offset:         288
        .size:           2
        .value_kind:     hidden_group_size_z
      - .offset:         290
        .size:           2
        .value_kind:     hidden_remainder_x
      - .offset:         292
        .size:           2
        .value_kind:     hidden_remainder_y
      - .offset:         294
        .size:           2
        .value_kind:     hidden_remainder_z
      - .offset:         312
        .size:           8
        .value_kind:     hidden_global_offset_x
      - .offset:         320
        .size:           8
        .value_kind:     hidden_global_offset_y
      - .offset:         328
        .size:           8
        .value_kind:     hidden_global_offset_z
      - .offset:         336
        .size:           2
        .value_kind:     hidden_grid_dims
      - .offset:         392
        .size:           4
        .value_kind:     hidden_dynamic_lds_size
    .group_segment_fixed_size: 0
    .kernarg_segment_align: 8
    .kernarg_segment_size: 528
    .language:       OpenCL C
    .language_version:
      - 2
      - 0
    .max_flat_workgroup_size: 512
    .name:           _Z10fwd_kernel4Args
    .private_segment_fixed_size: 0
    .sgpr_count:     108
    .sgpr_spill_count: 22
    .symbol:         _Z10fwd_kernel4Args.kd
    .uniform_work_group_size: 1
    .uses_dynamic_stack: false
    .vgpr_count:     255
    .vgpr_spill_count: 0
    .wavefront_size: 64
